# conv_experts balance variant: 6 tiles per job handed from workgroups 0..127 to w+128; plus exp1 preamble tables
# baseline (speedup 1.0000x reference)
.LBB0_2820:
	s_add_i32 s43, s44, s93
	s_movk_i32 s32, 0xfff
	s_bitcmp0_b32 s92, 7
	s_cselect_b32 s32, 0x9ff, s32
	s_cmp_gt_i32 s43, s32
	s_cbranch_scc0 .Lcbal0_go
	s_bitcmp1_b32 s44, 7
	s_cbranch_scc0 .Lcbal0_done
	s_add_i32 s43, s44, 0xfffffa80
	s_cmp_gt_i32 s43, 0xfff
	s_branch .Lcbal0_go

.LBB0_2834:
	s_add_i32 s41, s42, s93
	s_movk_i32 s32, 0xfff
	s_bitcmp0_b32 s92, 7
	s_cselect_b32 s32, 0x9ff, s32
	s_cmp_gt_i32 s41, s32
	s_cbranch_scc0 .Lcbal2_go
	s_bitcmp1_b32 s42, 7
	s_cbranch_scc0 .Lcbal2_done
	s_add_i32 s41, s42, 0xfffffa80
	s_cmp_gt_i32 s41, 0xfff
	s_branch .Lcbal2_go
